# scatter: histogram-matrix read rewritten with 60 rows in flight per thread (one memory round trip instead of two dependent batches), scalar-branch prefix split
# speedup vs baseline: 1.0268x; 1.0268x over previous
_Z14scatter_kernelPKiS0_S0_PiP15HIP_vector_typeIiLj2EE:
	s_load_dwordx4 s[52:55], s[0:1], 0x0
	s_load_dwordx4 s[12:15], s[0:1], 0x18
	s_movk_i32 s3, 0x31f
	v_cmp_lt_u32_e64 s[4:5], s3, v0
	s_movk_i32 s3, 0x320
	v_cmp_gt_u32_e32 vcc, s3, v0
	v_mov_b32_e32 v80, 0
	v_lshlrev_b32_e32 v2, 3, v0
	v_mov_b32_e32 v1, 0
	v_mov_b32_e32 v79, 0
	v_mov_b32_e32 v78, 0
	v_mov_b32_e32 v3, 0
	v_mov_b32_e32 v81, 0
	s_and_saveexec_b64 s[10:11], vcc
	s_cbranch_execz .LBB1_3
	s_load_dwordx2 s[6:7], s[0:1], 0x10
	s_waitcnt lgkmcnt(0)
	global_load_dwordx2 v[4:5], v2, s[6:7]
	s_add_u32 s6, s6, 0x1900
	s_addc_u32 s7, s7, 0
	global_load_dwordx2 v[6:7], v2, s[6:7]
	s_add_u32 s6, s6, 0x1900
	s_addc_u32 s7, s7, 0
	global_load_dwordx2 v[8:9], v2, s[6:7]
	s_add_u32 s6, s6, 0x1900
	s_addc_u32 s7, s7, 0
	global_load_dwordx2 v[10:11], v2, s[6:7]
	s_add_u32 s6, s6, 0x1900
	s_addc_u32 s7, s7, 0
	global_load_dwordx2 v[12:13], v2, s[6:7]
	s_add_u32 s6, s6, 0x1900
	s_addc_u32 s7, s7, 0
	global_load_dwordx2 v[14:15], v2, s[6:7]
	s_add_u32 s6, s6, 0x1900
	s_addc_u32 s7, s7, 0
	global_load_dwordx2 v[16:17], v2, s[6:7]
	s_add_u32 s6, s6, 0x1900
	s_addc_u32 s7, s7, 0
	global_load_dwordx2 v[18:19], v2, s[6:7]
	s_add_u32 s6, s6, 0x1900
	s_addc_u32 s7, s7, 0
	global_load_dwordx2 v[20:21], v2, s[6:7]
	s_add_u32 s6, s6, 0x1900
	s_addc_u32 s7, s7, 0
	global_load_dwordx2 v[22:23], v2, s[6:7]
	s_add_u32 s6, s6, 0x1900
	s_addc_u32 s7, s7, 0
	global_load_dwordx2 v[24:25], v2, s[6:7]
	s_add_u32 s6, s6, 0x1900
	s_addc_u32 s7, s7, 0
	global_load_dwordx2 v[26:27], v2, s[6:7]
	s_add_u32 s6, s6, 0x1900
	s_addc_u32 s7, s7, 0
	global_load_dwordx2 v[28:29], v2, s[6:7]
	s_add_u32 s6, s6, 0x1900
	s_addc_u32 s7, s7, 0
	global_load_dwordx2 v[30:31], v2, s[6:7]
	s_add_u32 s6, s6, 0x1900
	s_addc_u32 s7, s7, 0
	global_load_dwordx2 v[32:33], v2, s[6:7]
	s_add_u32 s6, s6, 0x1900
	s_addc_u32 s7, s7, 0
	global_load_dwordx2 v[34:35], v2, s[6:7]
	s_add_u32 s6, s6, 0x1900
	s_addc_u32 s7, s7, 0
	global_load_dwordx2 v[36:37], v2, s[6:7]
	s_add_u32 s6, s6, 0x1900
	s_addc_u32 s7, s7, 0
	global_load_dwordx2 v[38:39], v2, s[6:7]
	s_add_u32 s6, s6, 0x1900
	s_addc_u32 s7, s7, 0
	global_load_dwordx2 v[40:41], v2, s[6:7]
	s_add_u32 s6, s6, 0x1900
	s_addc_u32 s7, s7, 0
	global_load_dwordx2 v[42:43], v2, s[6:7]
	s_add_u32 s6, s6, 0x1900
	s_addc_u32 s7, s7, 0
	global_load_dwordx2 v[44:45], v2, s[6:7]
	s_add_u32 s6, s6, 0x1900
	s_addc_u32 s7, s7, 0
	global_load_dwordx2 v[46:47], v2, s[6:7]
	s_add_u32 s6, s6, 0x1900
	s_addc_u32 s7, s7, 0
	global_load_dwordx2 v[48:49], v2, s[6:7]
	s_add_u32 s6, s6, 0x1900
	s_addc_u32 s7, s7, 0
	global_load_dwordx2 v[50:51], v2, s[6:7]
	s_add_u32 s6, s6, 0x1900
	s_addc_u32 s7, s7, 0
	global_load_dwordx2 v[52:53], v2, s[6:7]
	s_add_u32 s6, s6, 0x1900
	s_addc_u32 s7, s7, 0
	global_load_dwordx2 v[54:55], v2, s[6:7]
	s_add_u32 s6, s6, 0x1900
	s_addc_u32 s7, s7, 0
	global_load_dwordx2 v[56:57], v2, s[6:7]
	s_add_u32 s6, s6, 0x1900
	s_addc_u32 s7, s7, 0
	global_load_dwordx2 v[58:59], v2, s[6:7]
	s_add_u32 s6, s6, 0x1900
	s_addc_u32 s7, s7, 0
	global_load_dwordx2 v[60:61], v2, s[6:7]
	s_add_u32 s6, s6, 0x1900
	s_addc_u32 s7, s7, 0
	global_load_dwordx2 v[62:63], v2, s[6:7]
	s_add_u32 s6, s6, 0x1900
	s_addc_u32 s7, s7, 0
	global_load_dwordx2 v[64:65], v2, s[6:7]
	s_add_u32 s6, s6, 0x1900
	s_addc_u32 s7, s7, 0
	global_load_dwordx2 v[66:67], v2, s[6:7]
	s_add_u32 s6, s6, 0x1900
	s_addc_u32 s7, s7, 0
	global_load_dwordx2 v[68:69], v2, s[6:7]
	s_add_u32 s6, s6, 0x1900
	s_addc_u32 s7, s7, 0
	global_load_dwordx2 v[70:71], v2, s[6:7]
	s_add_u32 s6, s6, 0x1900
	s_addc_u32 s7, s7, 0
	global_load_dwordx2 v[72:73], v2, s[6:7]
	s_add_u32 s6, s6, 0x1900
	s_addc_u32 s7, s7, 0
	global_load_dwordx2 v[74:75], v2, s[6:7]
	s_add_u32 s6, s6, 0x1900
	s_addc_u32 s7, s7, 0
	global_load_dwordx2 v[76:77], v2, s[6:7]
	s_add_u32 s6, s6, 0x1900
	s_addc_u32 s7, s7, 0
	global_load_dwordx2 v[82:83], v2, s[6:7]
	s_add_u32 s6, s6, 0x1900
	s_addc_u32 s7, s7, 0
	global_load_dwordx2 v[84:85], v2, s[6:7]
	s_add_u32 s6, s6, 0x1900
	s_addc_u32 s7, s7, 0
	global_load_dwordx2 v[86:87], v2, s[6:7]
	s_add_u32 s6, s6, 0x1900
	s_addc_u32 s7, s7, 0
	global_load_dwordx2 v[88:89], v2, s[6:7]
	s_add_u32 s6, s6, 0x1900
	s_addc_u32 s7, s7, 0
	global_load_dwordx2 v[90:91], v2, s[6:7]
	s_add_u32 s6, s6, 0x1900
	s_addc_u32 s7, s7, 0
	global_load_dwordx2 v[92:93], v2, s[6:7]
	s_add_u32 s6, s6, 0x1900
	s_addc_u32 s7, s7, 0
	global_load_dwordx2 v[94:95], v2, s[6:7]
	s_add_u32 s6, s6, 0x1900
	s_addc_u32 s7, s7, 0
	global_load_dwordx2 v[96:97], v2, s[6:7]
	s_add_u32 s6, s6, 0x1900
	s_addc_u32 s7, s7, 0
	global_load_dwordx2 v[98:99], v2, s[6:7]
	s_add_u32 s6, s6, 0x1900
	s_addc_u32 s7, s7, 0
	global_load_dwordx2 v[100:101], v2, s[6:7]
	s_add_u32 s6, s6, 0x1900
	s_addc_u32 s7, s7, 0
	global_load_dwordx2 v[102:103], v2, s[6:7]
	s_add_u32 s6, s6, 0x1900
	s_addc_u32 s7, s7, 0
	global_load_dwordx2 v[104:105], v2, s[6:7]
	s_add_u32 s6, s6, 0x1900
	s_addc_u32 s7, s7, 0
	global_load_dwordx2 v[106:107], v2, s[6:7]
	s_add_u32 s6, s6, 0x1900
	s_addc_u32 s7, s7, 0
	global_load_dwordx2 v[108:109], v2, s[6:7]
	s_add_u32 s6, s6, 0x1900
	s_addc_u32 s7, s7, 0
	global_load_dwordx2 v[110:111], v2, s[6:7]
	s_add_u32 s6, s6, 0x1900
	s_addc_u32 s7, s7, 0
	global_load_dwordx2 v[112:113], v2, s[6:7]
	s_add_u32 s6, s6, 0x1900
	s_addc_u32 s7, s7, 0
	global_load_dwordx2 v[114:115], v2, s[6:7]
	s_add_u32 s6, s6, 0x1900
	s_addc_u32 s7, s7, 0
	global_load_dwordx2 v[116:117], v2, s[6:7]
	s_add_u32 s6, s6, 0x1900
	s_addc_u32 s7, s7, 0
	global_load_dwordx2 v[118:119], v2, s[6:7]
	s_add_u32 s6, s6, 0x1900
	s_addc_u32 s7, s7, 0
	global_load_dwordx2 v[120:121], v2, s[6:7]
	s_add_u32 s6, s6, 0x1900
	s_addc_u32 s7, s7, 0
	global_load_dwordx2 v[122:123], v2, s[6:7]
	s_add_u32 s6, s6, 0x1900
	s_addc_u32 s7, s7, 0
	global_load_dwordx2 v[124:125], v2, s[6:7]
	s_add_u32 s6, s6, 0x1900
	s_addc_u32 s7, s7, 0
	global_load_dwordx2 v[126:127], v2, s[6:7]
	s_add_u32 s6, s6, 0x1900
	s_addc_u32 s7, s7, 0
	s_waitcnt vmcnt(59)
	s_cmp_eq_u32 s2, 0
	s_cbranch_scc0 .Lsc_h0
	v_mov_b32_e32 v79, v1
	v_mov_b32_e32 v78, v80
	v_mov_b32_e32 v3, v4
	v_mov_b32_e32 v81, v5
.Lsc_h0:
	v_add_u32_e32 v1, v1, v4
	v_add_u32_e32 v80, v80, v5
	global_load_dwordx2 v[4:5], v2, s[6:7]
	s_add_u32 s6, s6, 0x1900
	s_addc_u32 s7, s7, 0
	s_waitcnt vmcnt(59)
	s_cmp_eq_u32 s2, 1
	s_cbranch_scc0 .Lsc_h1
	v_mov_b32_e32 v79, v1
	v_mov_b32_e32 v78, v80
	v_mov_b32_e32 v3, v6
	v_mov_b32_e32 v81, v7
.Lsc_h1:
	v_add_u32_e32 v1, v1, v6
	v_add_u32_e32 v80, v80, v7
	global_load_dwordx2 v[6:7], v2, s[6:7]
	s_add_u32 s6, s6, 0x1900
	s_addc_u32 s7, s7, 0
	s_waitcnt vmcnt(59)
	s_cmp_eq_u32 s2, 2
	s_cbranch_scc0 .Lsc_h2
	v_mov_b32_e32 v79, v1
	v_mov_b32_e32 v78, v80
	v_mov_b32_e32 v3, v8
	v_mov_b32_e32 v81, v9
.Lsc_h2:
	v_add_u32_e32 v1, v1, v8
	v_add_u32_e32 v80, v80, v9
	global_load_dwordx2 v[8:9], v2, s[6:7]
	s_add_u32 s6, s6, 0x1900
	s_addc_u32 s7, s7, 0
	s_waitcnt vmcnt(59)
	s_cmp_eq_u32 s2, 3
	s_cbranch_scc0 .Lsc_h3
	v_mov_b32_e32 v79, v1
	v_mov_b32_e32 v78, v80
	v_mov_b32_e32 v3, v10
	v_mov_b32_e32 v81, v11
.Lsc_h3:
	v_add_u32_e32 v1, v1, v10
	v_add_u32_e32 v80, v80, v11
	global_load_dwordx2 v[10:11], v2, s[6:7]
	s_add_u32 s6, s6, 0x1900
	s_addc_u32 s7, s7, 0
	s_waitcnt vmcnt(59)
	s_cmp_eq_u32 s2, 4
	s_cbranch_scc0 .Lsc_h4
	v_mov_b32_e32 v79, v1
	v_mov_b32_e32 v78, v80
	v_mov_b32_e32 v3, v12
	v_mov_b32_e32 v81, v13
.Lsc_h4:
	v_add_u32_e32 v1, v1, v12
	v_add_u32_e32 v80, v80, v13
	s_waitcnt vmcnt(58)
	s_cmp_eq_u32 s2, 5
	s_cbranch_scc0 .Lsc_h5
	v_mov_b32_e32 v79, v1
	v_mov_b32_e32 v78, v80
	v_mov_b32_e32 v3, v14
	v_mov_b32_e32 v81, v15
.Lsc_h5:
	v_add_u32_e32 v1, v1, v14
	v_add_u32_e32 v80, v80, v15
	s_waitcnt vmcnt(57)
	s_cmp_eq_u32 s2, 6
	s_cbranch_scc0 .Lsc_h6
	v_mov_b32_e32 v79, v1
	v_mov_b32_e32 v78, v80
	v_mov_b32_e32 v3, v16
	v_mov_b32_e32 v81, v17
.Lsc_h6:
	v_add_u32_e32 v1, v1, v16
	v_add_u32_e32 v80, v80, v17
	s_waitcnt vmcnt(56)
	s_cmp_eq_u32 s2, 7
	s_cbranch_scc0 .Lsc_h7
	v_mov_b32_e32 v79, v1
	v_mov_b32_e32 v78, v80
	v_mov_b32_e32 v3, v18
	v_mov_b32_e32 v81, v19
.Lsc_h7:
	v_add_u32_e32 v1, v1, v18
	v_add_u32_e32 v80, v80, v19
	s_waitcnt vmcnt(55)
	s_cmp_eq_u32 s2, 8
	s_cbranch_scc0 .Lsc_h8
	v_mov_b32_e32 v79, v1
	v_mov_b32_e32 v78, v80
	v_mov_b32_e32 v3, v20
	v_mov_b32_e32 v81, v21
.Lsc_h8:
	v_add_u32_e32 v1, v1, v20
	v_add_u32_e32 v80, v80, v21
	s_waitcnt vmcnt(54)
	s_cmp_eq_u32 s2, 9
	s_cbranch_scc0 .Lsc_h9
	v_mov_b32_e32 v79, v1
	v_mov_b32_e32 v78, v80
	v_mov_b32_e32 v3, v22
	v_mov_b32_e32 v81, v23
.Lsc_h9:
	v_add_u32_e32 v1, v1, v22
	v_add_u32_e32 v80, v80, v23
	s_waitcnt vmcnt(53)
	s_cmp_eq_u32 s2, 10
	s_cbranch_scc0 .Lsc_h10
	v_mov_b32_e32 v79, v1
	v_mov_b32_e32 v78, v80
	v_mov_b32_e32 v3, v24
	v_mov_b32_e32 v81, v25
.Lsc_h10:
	v_add_u32_e32 v1, v1, v24
	v_add_u32_e32 v80, v80, v25
	s_waitcnt vmcnt(52)
	s_cmp_eq_u32 s2, 11
	s_cbranch_scc0 .Lsc_h11
	v_mov_b32_e32 v79, v1
	v_mov_b32_e32 v78, v80
	v_mov_b32_e32 v3, v26
	v_mov_b32_e32 v81, v27
.Lsc_h11:
	v_add_u32_e32 v1, v1, v26
	v_add_u32_e32 v80, v80, v27
	s_waitcnt vmcnt(51)
	s_cmp_eq_u32 s2, 12
	s_cbranch_scc0 .Lsc_h12
	v_mov_b32_e32 v79, v1
	v_mov_b32_e32 v78, v80
	v_mov_b32_e32 v3, v28
	v_mov_b32_e32 v81, v29
.Lsc_h12:
	v_add_u32_e32 v1, v1, v28
	v_add_u32_e32 v80, v80, v29
	s_waitcnt vmcnt(50)
	s_cmp_eq_u32 s2, 13
	s_cbranch_scc0 .Lsc_h13
	v_mov_b32_e32 v79, v1
	v_mov_b32_e32 v78, v80
	v_mov_b32_e32 v3, v30
	v_mov_b32_e32 v81, v31
.Lsc_h13:
	v_add_u32_e32 v1, v1, v30
	v_add_u32_e32 v80, v80, v31
	s_waitcnt vmcnt(49)
	s_cmp_eq_u32 s2, 14
	s_cbranch_scc0 .Lsc_h14
	v_mov_b32_e32 v79, v1
	v_mov_b32_e32 v78, v80
	v_mov_b32_e32 v3, v32
	v_mov_b32_e32 v81, v33
.Lsc_h14:
	v_add_u32_e32 v1, v1, v32
	v_add_u32_e32 v80, v80, v33
	s_waitcnt vmcnt(48)
	s_cmp_eq_u32 s2, 15
	s_cbranch_scc0 .Lsc_h15
	v_mov_b32_e32 v79, v1
	v_mov_b32_e32 v78, v80
	v_mov_b32_e32 v3, v34
	v_mov_b32_e32 v81, v35
.Lsc_h15:
	v_add_u32_e32 v1, v1, v34
	v_add_u32_e32 v80, v80, v35
	s_waitcnt vmcnt(47)
	s_cmp_eq_u32 s2, 16
	s_cbranch_scc0 .Lsc_h16
	v_mov_b32_e32 v79, v1
	v_mov_b32_e32 v78, v80
	v_mov_b32_e32 v3, v36
	v_mov_b32_e32 v81, v37
.Lsc_h16:
	v_add_u32_e32 v1, v1, v36
	v_add_u32_e32 v80, v80, v37
	s_waitcnt vmcnt(46)
	s_cmp_eq_u32 s2, 17
	s_cbranch_scc0 .Lsc_h17
	v_mov_b32_e32 v79, v1
	v_mov_b32_e32 v78, v80
	v_mov_b32_e32 v3, v38
	v_mov_b32_e32 v81, v39
.Lsc_h17:
	v_add_u32_e32 v1, v1, v38
	v_add_u32_e32 v80, v80, v39
	s_waitcnt vmcnt(45)
	s_cmp_eq_u32 s2, 18
	s_cbranch_scc0 .Lsc_h18
	v_mov_b32_e32 v79, v1
	v_mov_b32_e32 v78, v80
	v_mov_b32_e32 v3, v40
	v_mov_b32_e32 v81, v41
.Lsc_h18:
	v_add_u32_e32 v1, v1, v40
	v_add_u32_e32 v80, v80, v41
	s_waitcnt vmcnt(44)
	s_cmp_eq_u32 s2, 19
	s_cbranch_scc0 .Lsc_h19
	v_mov_b32_e32 v79, v1
	v_mov_b32_e32 v78, v80
	v_mov_b32_e32 v3, v42
	v_mov_b32_e32 v81, v43
.Lsc_h19:
	v_add_u32_e32 v1, v1, v42
	v_add_u32_e32 v80, v80, v43
	s_waitcnt vmcnt(43)
	s_cmp_eq_u32 s2, 20
	s_cbranch_scc0 .Lsc_h20
	v_mov_b32_e32 v79, v1
	v_mov_b32_e32 v78, v80
	v_mov_b32_e32 v3, v44
	v_mov_b32_e32 v81, v45
.Lsc_h20:
	v_add_u32_e32 v1, v1, v44
	v_add_u32_e32 v80, v80, v45
	s_waitcnt vmcnt(42)
	s_cmp_eq_u32 s2, 21
	s_cbranch_scc0 .Lsc_h21
	v_mov_b32_e32 v79, v1
	v_mov_b32_e32 v78, v80
	v_mov_b32_e32 v3, v46
	v_mov_b32_e32 v81, v47
.Lsc_h21:
	v_add_u32_e32 v1, v1, v46
	v_add_u32_e32 v80, v80, v47
	s_waitcnt vmcnt(41)
	s_cmp_eq_u32 s2, 22
	s_cbranch_scc0 .Lsc_h22
	v_mov_b32_e32 v79, v1
	v_mov_b32_e32 v78, v80
	v_mov_b32_e32 v3, v48
	v_mov_b32_e32 v81, v49
.Lsc_h22:
	v_add_u32_e32 v1, v1, v48
	v_add_u32_e32 v80, v80, v49
	s_waitcnt vmcnt(40)
	s_cmp_eq_u32 s2, 23
	s_cbranch_scc0 .Lsc_h23
	v_mov_b32_e32 v79, v1
	v_mov_b32_e32 v78, v80
	v_mov_b32_e32 v3, v50
	v_mov_b32_e32 v81, v51
.Lsc_h23:
	v_add_u32_e32 v1, v1, v50
	v_add_u32_e32 v80, v80, v51
	s_waitcnt vmcnt(39)
	s_cmp_eq_u32 s2, 24
	s_cbranch_scc0 .Lsc_h24
	v_mov_b32_e32 v79, v1
	v_mov_b32_e32 v78, v80
	v_mov_b32_e32 v3, v52
	v_mov_b32_e32 v81, v53
.Lsc_h24:
	v_add_u32_e32 v1, v1, v52
	v_add_u32_e32 v80, v80, v53
	s_waitcnt vmcnt(38)
	s_cmp_eq_u32 s2, 25
	s_cbranch_scc0 .Lsc_h25
	v_mov_b32_e32 v79, v1
	v_mov_b32_e32 v78, v80
	v_mov_b32_e32 v3, v54
	v_mov_b32_e32 v81, v55
.Lsc_h25:
	v_add_u32_e32 v1, v1, v54
	v_add_u32_e32 v80, v80, v55
	s_waitcnt vmcnt(37)
	s_cmp_eq_u32 s2, 26
	s_cbranch_scc0 .Lsc_h26
	v_mov_b32_e32 v79, v1
	v_mov_b32_e32 v78, v80
	v_mov_b32_e32 v3, v56
	v_mov_b32_e32 v81, v57
.Lsc_h26:
	v_add_u32_e32 v1, v1, v56
	v_add_u32_e32 v80, v80, v57
	s_waitcnt vmcnt(36)
	s_cmp_eq_u32 s2, 27
	s_cbranch_scc0 .Lsc_h27
	v_mov_b32_e32 v79, v1
	v_mov_b32_e32 v78, v80
	v_mov_b32_e32 v3, v58
	v_mov_b32_e32 v81, v59
.Lsc_h27:
	v_add_u32_e32 v1, v1, v58
	v_add_u32_e32 v80, v80, v59
	s_waitcnt vmcnt(35)
	s_cmp_eq_u32 s2, 28
	s_cbranch_scc0 .Lsc_h28
	v_mov_b32_e32 v79, v1
	v_mov_b32_e32 v78, v80
	v_mov_b32_e32 v3, v60
	v_mov_b32_e32 v81, v61
.Lsc_h28:
	v_add_u32_e32 v1, v1, v60
	v_add_u32_e32 v80, v80, v61
	s_waitcnt vmcnt(34)
	s_cmp_eq_u32 s2, 29
	s_cbranch_scc0 .Lsc_h29
	v_mov_b32_e32 v79, v1
	v_mov_b32_e32 v78, v80
	v_mov_b32_e32 v3, v62
	v_mov_b32_e32 v81, v63
.Lsc_h29:
	v_add_u32_e32 v1, v1, v62
	v_add_u32_e32 v80, v80, v63
	s_waitcnt vmcnt(33)
	s_cmp_eq_u32 s2, 30
	s_cbranch_scc0 .Lsc_h30
	v_mov_b32_e32 v79, v1
	v_mov_b32_e32 v78, v80
	v_mov_b32_e32 v3, v64
	v_mov_b32_e32 v81, v65
.Lsc_h30:
	v_add_u32_e32 v1, v1, v64
	v_add_u32_e32 v80, v80, v65
	s_waitcnt vmcnt(32)
	s_cmp_eq_u32 s2, 31
	s_cbranch_scc0 .Lsc_h31
	v_mov_b32_e32 v79, v1
	v_mov_b32_e32 v78, v80
	v_mov_b32_e32 v3, v66
	v_mov_b32_e32 v81, v67
.Lsc_h31:
	v_add_u32_e32 v1, v1, v66
	v_add_u32_e32 v80, v80, v67
	s_waitcnt vmcnt(31)
	s_cmp_eq_u32 s2, 32
	s_cbranch_scc0 .Lsc_h32
	v_mov_b32_e32 v79, v1
	v_mov_b32_e32 v78, v80
	v_mov_b32_e32 v3, v68
	v_mov_b32_e32 v81, v69
.Lsc_h32:
	v_add_u32_e32 v1, v1, v68
	v_add_u32_e32 v80, v80, v69
	s_waitcnt vmcnt(30)
	s_cmp_eq_u32 s2, 33
	s_cbranch_scc0 .Lsc_h33
	v_mov_b32_e32 v79, v1
	v_mov_b32_e32 v78, v80
	v_mov_b32_e32 v3, v70
	v_mov_b32_e32 v81, v71
.Lsc_h33:
	v_add_u32_e32 v1, v1, v70
	v_add_u32_e32 v80, v80, v71
	s_waitcnt vmcnt(29)
	s_cmp_eq_u32 s2, 34
	s_cbranch_scc0 .Lsc_h34
	v_mov_b32_e32 v79, v1
	v_mov_b32_e32 v78, v80
	v_mov_b32_e32 v3, v72
	v_mov_b32_e32 v81, v73
.Lsc_h34:
	v_add_u32_e32 v1, v1, v72
	v_add_u32_e32 v80, v80, v73
	s_waitcnt vmcnt(28)
	s_cmp_eq_u32 s2, 35
	s_cbranch_scc0 .Lsc_h35
	v_mov_b32_e32 v79, v1
	v_mov_b32_e32 v78, v80
	v_mov_b32_e32 v3, v74
	v_mov_b32_e32 v81, v75
.Lsc_h35:
	v_add_u32_e32 v1, v1, v74
	v_add_u32_e32 v80, v80, v75
	s_waitcnt vmcnt(27)
	s_cmp_eq_u32 s2, 36
	s_cbranch_scc0 .Lsc_h36
	v_mov_b32_e32 v79, v1
	v_mov_b32_e32 v78, v80
	v_mov_b32_e32 v3, v76
	v_mov_b32_e32 v81, v77
.Lsc_h36:
	v_add_u32_e32 v1, v1, v76
	v_add_u32_e32 v80, v80, v77
	s_waitcnt vmcnt(26)
	s_cmp_eq_u32 s2, 37
	s_cbranch_scc0 .Lsc_h37
	v_mov_b32_e32 v79, v1
	v_mov_b32_e32 v78, v80
	v_mov_b32_e32 v3, v82
	v_mov_b32_e32 v81, v83
.Lsc_h37:
	v_add_u32_e32 v1, v1, v82
	v_add_u32_e32 v80, v80, v83
	s_waitcnt vmcnt(25)
	s_cmp_eq_u32 s2, 38
	s_cbranch_scc0 .Lsc_h38
	v_mov_b32_e32 v79, v1
	v_mov_b32_e32 v78, v80
	v_mov_b32_e32 v3, v84
	v_mov_b32_e32 v81, v85
.Lsc_h38:
	v_add_u32_e32 v1, v1, v84
	v_add_u32_e32 v80, v80, v85
	s_waitcnt vmcnt(24)
	s_cmp_eq_u32 s2, 39
	s_cbranch_scc0 .Lsc_h39
	v_mov_b32_e32 v79, v1
	v_mov_b32_e32 v78, v80
	v_mov_b32_e32 v3, v86
	v_mov_b32_e32 v81, v87
.Lsc_h39:
	v_add_u32_e32 v1, v1, v86
	v_add_u32_e32 v80, v80, v87
	s_waitcnt vmcnt(23)
	s_cmp_eq_u32 s2, 40
	s_cbranch_scc0 .Lsc_h40
	v_mov_b32_e32 v79, v1
	v_mov_b32_e32 v78, v80
	v_mov_b32_e32 v3, v88
	v_mov_b32_e32 v81, v89
.Lsc_h40:
	v_add_u32_e32 v1, v1, v88
	v_add_u32_e32 v80, v80, v89
	s_waitcnt vmcnt(22)
	s_cmp_eq_u32 s2, 41
	s_cbranch_scc0 .Lsc_h41
	v_mov_b32_e32 v79, v1
	v_mov_b32_e32 v78, v80
	v_mov_b32_e32 v3, v90
	v_mov_b32_e32 v81, v91
.Lsc_h41:
	v_add_u32_e32 v1, v1, v90
	v_add_u32_e32 v80, v80, v91
	s_waitcnt vmcnt(21)
	s_cmp_eq_u32 s2, 42
	s_cbranch_scc0 .Lsc_h42
	v_mov_b32_e32 v79, v1
	v_mov_b32_e32 v78, v80
	v_mov_b32_e32 v3, v92
	v_mov_b32_e32 v81, v93
.Lsc_h42:
	v_add_u32_e32 v1, v1, v92
	v_add_u32_e32 v80, v80, v93
	s_waitcnt vmcnt(20)
	s_cmp_eq_u32 s2, 43
	s_cbranch_scc0 .Lsc_h43
	v_mov_b32_e32 v79, v1
	v_mov_b32_e32 v78, v80
	v_mov_b32_e32 v3, v94
	v_mov_b32_e32 v81, v95
.Lsc_h43:
	v_add_u32_e32 v1, v1, v94
	v_add_u32_e32 v80, v80, v95
	s_waitcnt vmcnt(19)
	s_cmp_eq_u32 s2, 44
	s_cbranch_scc0 .Lsc_h44
	v_mov_b32_e32 v79, v1
	v_mov_b32_e32 v78, v80
	v_mov_b32_e32 v3, v96
	v_mov_b32_e32 v81, v97
.Lsc_h44:
	v_add_u32_e32 v1, v1, v96
	v_add_u32_e32 v80, v80, v97
	s_waitcnt vmcnt(18)
	s_cmp_eq_u32 s2, 45
	s_cbranch_scc0 .Lsc_h45
	v_mov_b32_e32 v79, v1
	v_mov_b32_e32 v78, v80
	v_mov_b32_e32 v3, v98
	v_mov_b32_e32 v81, v99
.Lsc_h45:
	v_add_u32_e32 v1, v1, v98
	v_add_u32_e32 v80, v80, v99
	s_waitcnt vmcnt(17)
	s_cmp_eq_u32 s2, 46
	s_cbranch_scc0 .Lsc_h46
	v_mov_b32_e32 v79, v1
	v_mov_b32_e32 v78, v80
	v_mov_b32_e32 v3, v100
	v_mov_b32_e32 v81, v101
.Lsc_h46:
	v_add_u32_e32 v1, v1, v100
	v_add_u32_e32 v80, v80, v101
	s_waitcnt vmcnt(16)
	s_cmp_eq_u32 s2, 47
	s_cbranch_scc0 .Lsc_h47
	v_mov_b32_e32 v79, v1
	v_mov_b32_e32 v78, v80
	v_mov_b32_e32 v3, v102
	v_mov_b32_e32 v81, v103
.Lsc_h47:
	v_add_u32_e32 v1, v1, v102
	v_add_u32_e32 v80, v80, v103
	s_waitcnt vmcnt(15)
	s_cmp_eq_u32 s2, 48
	s_cbranch_scc0 .Lsc_h48
	v_mov_b32_e32 v79, v1
	v_mov_b32_e32 v78, v80
	v_mov_b32_e32 v3, v104
	v_mov_b32_e32 v81, v105
.Lsc_h48:
	v_add_u32_e32 v1, v1, v104
	v_add_u32_e32 v80, v80, v105
	s_waitcnt vmcnt(14)
	s_cmp_eq_u32 s2, 49
	s_cbranch_scc0 .Lsc_h49
	v_mov_b32_e32 v79, v1
	v_mov_b32_e32 v78, v80
	v_mov_b32_e32 v3, v106
	v_mov_b32_e32 v81, v107
.Lsc_h49:
	v_add_u32_e32 v1, v1, v106
	v_add_u32_e32 v80, v80, v107
	s_waitcnt vmcnt(13)
	s_cmp_eq_u32 s2, 50
	s_cbranch_scc0 .Lsc_h50
	v_mov_b32_e32 v79, v1
	v_mov_b32_e32 v78, v80
	v_mov_b32_e32 v3, v108
	v_mov_b32_e32 v81, v109
.Lsc_h50:
	v_add_u32_e32 v1, v1, v108
	v_add_u32_e32 v80, v80, v109
	s_waitcnt vmcnt(12)
	s_cmp_eq_u32 s2, 51
	s_cbranch_scc0 .Lsc_h51
	v_mov_b32_e32 v79, v1
	v_mov_b32_e32 v78, v80
	v_mov_b32_e32 v3, v110
	v_mov_b32_e32 v81, v111
.Lsc_h51:
	v_add_u32_e32 v1, v1, v110
	v_add_u32_e32 v80, v80, v111
	s_waitcnt vmcnt(11)
	s_cmp_eq_u32 s2, 52
	s_cbranch_scc0 .Lsc_h52
	v_mov_b32_e32 v79, v1
	v_mov_b32_e32 v78, v80
	v_mov_b32_e32 v3, v112
	v_mov_b32_e32 v81, v113
.Lsc_h52:
	v_add_u32_e32 v1, v1, v112
	v_add_u32_e32 v80, v80, v113
	s_waitcnt vmcnt(10)
	s_cmp_eq_u32 s2, 53
	s_cbranch_scc0 .Lsc_h53
	v_mov_b32_e32 v79, v1
	v_mov_b32_e32 v78, v80
	v_mov_b32_e32 v3, v114
	v_mov_b32_e32 v81, v115
.Lsc_h53:
	v_add_u32_e32 v1, v1, v114
	v_add_u32_e32 v80, v80, v115
	s_waitcnt vmcnt(9)
	s_cmp_eq_u32 s2, 54
	s_cbranch_scc0 .Lsc_h54
	v_mov_b32_e32 v79, v1
	v_mov_b32_e32 v78, v80
	v_mov_b32_e32 v3, v116
	v_mov_b32_e32 v81, v117
.Lsc_h54:
	v_add_u32_e32 v1, v1, v116
	v_add_u32_e32 v80, v80, v117
	s_waitcnt vmcnt(8)
	s_cmp_eq_u32 s2, 55
	s_cbranch_scc0 .Lsc_h55
	v_mov_b32_e32 v79, v1
	v_mov_b32_e32 v78, v80
	v_mov_b32_e32 v3, v118
	v_mov_b32_e32 v81, v119
.Lsc_h55:
	v_add_u32_e32 v1, v1, v118
	v_add_u32_e32 v80, v80, v119
	s_waitcnt vmcnt(7)
	s_cmp_eq_u32 s2, 56
	s_cbranch_scc0 .Lsc_h56
	v_mov_b32_e32 v79, v1
	v_mov_b32_e32 v78, v80
	v_mov_b32_e32 v3, v120
	v_mov_b32_e32 v81, v121
.Lsc_h56:
	v_add_u32_e32 v1, v1, v120
	v_add_u32_e32 v80, v80, v121
	s_waitcnt vmcnt(6)
	s_cmp_eq_u32 s2, 57
	s_cbranch_scc0 .Lsc_h57
	v_mov_b32_e32 v79, v1
	v_mov_b32_e32 v78, v80
	v_mov_b32_e32 v3, v122
	v_mov_b32_e32 v81, v123
.Lsc_h57:
	v_add_u32_e32 v1, v1, v122
	v_add_u32_e32 v80, v80, v123
	s_waitcnt vmcnt(5)
	s_cmp_eq_u32 s2, 58
	s_cbranch_scc0 .Lsc_h58
	v_mov_b32_e32 v79, v1
	v_mov_b32_e32 v78, v80
	v_mov_b32_e32 v3, v124
	v_mov_b32_e32 v81, v125
.Lsc_h58:
	v_add_u32_e32 v1, v1, v124
	v_add_u32_e32 v80, v80, v125
	s_waitcnt vmcnt(4)
	s_cmp_eq_u32 s2, 59
	s_cbranch_scc0 .Lsc_h59
	v_mov_b32_e32 v79, v1
	v_mov_b32_e32 v78, v80
	v_mov_b32_e32 v3, v126
	v_mov_b32_e32 v81, v127
.Lsc_h59:
	v_add_u32_e32 v1, v1, v126
	v_add_u32_e32 v80, v80, v127
	s_waitcnt vmcnt(3)
	s_cmp_eq_u32 s2, 60
	s_cbranch_scc0 .Lsc_h60
	v_mov_b32_e32 v79, v1
	v_mov_b32_e32 v78, v80
	v_mov_b32_e32 v3, v4
	v_mov_b32_e32 v81, v5
.Lsc_h60:
	v_add_u32_e32 v1, v1, v4
	v_add_u32_e32 v80, v80, v5
	s_waitcnt vmcnt(2)
	s_cmp_eq_u32 s2, 61
	s_cbranch_scc0 .Lsc_h61
	v_mov_b32_e32 v79, v1
	v_mov_b32_e32 v78, v80
	v_mov_b32_e32 v3, v6
	v_mov_b32_e32 v81, v7
.Lsc_h61:
	v_add_u32_e32 v1, v1, v6
	v_add_u32_e32 v80, v80, v7
	s_waitcnt vmcnt(1)
	s_cmp_eq_u32 s2, 62
	s_cbranch_scc0 .Lsc_h62
	v_mov_b32_e32 v79, v1
	v_mov_b32_e32 v78, v80
	v_mov_b32_e32 v3, v8
	v_mov_b32_e32 v81, v9
.Lsc_h62:
	v_add_u32_e32 v1, v1, v8
	v_add_u32_e32 v80, v80, v9
	s_waitcnt vmcnt(0)
	s_cmp_eq_u32 s2, 63
	s_cbranch_scc0 .Lsc_h63
	v_mov_b32_e32 v79, v1
	v_mov_b32_e32 v78, v80
	v_mov_b32_e32 v3, v10
	v_mov_b32_e32 v81, v11
.Lsc_h63:
	v_add_u32_e32 v1, v1, v10
	v_add_u32_e32 v80, v80, v11
